# edge0 gets the same XCD-aware tile assignment as edge1
# baseline (speedup 1.0000x reference)
.LBB3_4:
	s_or_b64 exec, exec, s[6:7]
	s_and_b32 s86, s2, 7
	s_lshl_b32 s86, s86, 4
	s_bfe_u32 s87, s2, 0x40003
	s_or_b32 s86, s86, s87
	s_and_b32 s87, s2, 0xffffff80
	s_or_b32 s2, s86, s87
	v_lshl_or_b32 v56, s2, 2, v32
	v_min_i32_e32 v32, 0x61a7, v56
	v_lshl_or_b32 v52, v32, 5, v62
	v_ashrrev_i32_e32 v53, 31, v52
	v_lshl_add_u64 v[58:59], v[52:53], 4, s[8:9]
	v_max_i32_e32 v32, 1, v52
	v_mov_b32_e32 v33, 0
	v_lshl_add_u64 v[60:61], v[32:33], 4, s[8:9]
	global_load_dwordx4 v[32:35], v[58:59], off
	global_load_dword v63, v[58:59], off offset:24
	global_load_dword v53, v[60:61], off offset:-8
	s_load_dword s6, s[0:1], 0x40
	s_waitcnt vmcnt(13)
	ds_write_b128 v30, v[14:17] offset:12800
	s_waitcnt vmcnt(12)
	ds_write_b128 v30, v[22:25] offset:16896
	s_waitcnt vmcnt(10)
	ds_write_b128 v30, v[48:51] offset:20992
	s_waitcnt vmcnt(9)
	v_cvt_f16_f32_e32 v14, v40
	v_cvt_f16_f32_e32 v15, v43
	v_cvt_pk_f16_f32 v17, v41, v42
	s_waitcnt vmcnt(8)
	v_cvt_f16_f32_e32 v23, v47
	v_pack_b32_f16 v16, v14, v17
	v_alignbit_b32 v17, v15, v17, 16
	v_cvt_f16_f32_e32 v15, v44
	v_cvt_pk_f16_f32 v24, v45, v46
	v_lshlrev_b32_e32 v14, 3, v0
	v_alignbit_b32 v23, v23, v24, 16
	v_pack_b32_f16 v22, v15, v24
	s_waitcnt vmcnt(7)
	v_cvt_f16_f32_e32 v15, v18
	ds_write2st64_b64 v14, v[16:17], v[22:23] offset1:4
	v_cvt_pk_f16_f32 v17, v19, v20
	v_cvt_f16_f32_e32 v18, v21
	v_pack_b32_f16 v16, v15, v17
	s_waitcnt vmcnt(6)
	v_cvt_f16_f32_e32 v15, v26
	v_cvt_f16_f32_e32 v19, v29
	s_waitcnt vmcnt(5)
	v_cvt_f16_f32_e32 v6, v6
	v_cvt_pk_f16_f32 v7, v7, v8
	v_cvt_f16_f32_e32 v8, v9
	s_waitcnt vmcnt(4)
	v_cvt_f16_f32_e32 v9, v10
	v_cvt_f16_f32_e32 v10, v13
	v_cvt_pk_f16_f32 v20, v27, v28
	v_cvt_pk_f16_f32 v11, v11, v12
	v_alignbit_b32 v17, v18, v17, 16
	v_pack_b32_f16 v18, v15, v20
	v_alignbit_b32 v19, v19, v20, 16
	v_pack_b32_f16 v6, v6, v7
	v_alignbit_b32 v7, v8, v7, 16
	v_pack_b32_f16 v8, v9, v11
	v_alignbit_b32 v9, v10, v11, 16
	ds_write_b128 v30, v[36:39] offset:25088
	ds_write2st64_b64 v14, v[16:17], v[18:19] offset0:8 offset1:12
	ds_write2st64_b64 v14, v[6:7], v[8:9] offset0:16 offset1:20
	s_and_saveexec_b64 s[2:3], vcc
	s_cbranch_execnz .LBB3_74
	s_or_b64 exec, exec, s[2:3]
	s_and_saveexec_b64 s[2:3], vcc
	s_cbranch_execnz .LBB3_75
